# GDN section d waves 1-7: fragment pieces rewritten (scalar fragment decode, all LDS reads first, one wait)
# speedup vs baseline: 1.0002x; 1.0002x over previous
.LBB0_329:
	v_readlane_b32 s20, v253, 43
	v_readlane_b32 s21, v253, 44
	s_mov_b64 s[0:1], -1
	s_and_b64 vcc, exec, s[20:21]
	s_waitcnt lgkmcnt(0)
	s_barrier
	s_cbranch_vccz .LBB0_338
	v_and_b32_e32 v0, 31, v215
	v_lshrrev_b32_e32 v1, 5, v215
	v_mul_u32_u24_e32 v2, 0x110, v0
	v_lshl_add_u32 v2, v1, 3, v2
	v_add_u32_e32 v2, 0x8800, v2
	v_lshlrev_b32_e32 v3, 2, v0
	v_add_u32_e32 v3, 0x1c600, v3
	v_mul_u32_u24_e32 v4, 0x440, v1
	v_lshl_add_u32 v4, v0, 1, v4
	v_lshlrev_b32_e32 v5, 4, v1
	v_add_u32_e32 v5, 0x1c700, v5
	v_lshlrev_b32_e32 v6, 4, v215
	s_add_i32 s34, s82, -1
	s_cmp_gt_u32 s34, 31
	s_cbranch_scc1 .Lgp_rd_done
	s_cmp_gt_u32 s34, 15
	s_cbranch_scc1 .Lgp_rk0
	s_lshr_b32 s20, s34, 3
	s_mul_i32 s21, s20, 0x2200
	s_lshl_b32 s22, s34, 5
	s_and_b32 s22, s22, 0xe0
	s_add_i32 s21, s21, s22
	v_add_u32_e32 v8, s21, v2
	ds_read2_b64 v[16:19], v8 offset1:2
	s_lshl_b32 s20, s20, 7
	v_add_u32_e32 v9, s20, v3
	ds_read_b32 v20, v9
	s_branch .Lgp_rn0
.Lgp_rk0:
	s_and_b32 s20, s34, 3
	s_mul_i32 s21, s20, 0x1100
	s_bfe_u32 s22, s34, 0x20002
	s_lshl_b32 s23, s22, 6
	s_add_i32 s21, s21, s23
	v_add_u32_e32 v8, s21, v4
	ds_read_u16 v16, v8
	ds_read_u16 v17, v8 offset:272
	ds_read_u16 v18, v8 offset:544
	ds_read_u16 v19, v8 offset:816
	ds_read_u16 v20, v8 offset:2176
	ds_read_u16 v21, v8 offset:2448
	ds_read_u16 v22, v8 offset:2720
	ds_read_u16 v23, v8 offset:2992
	s_lshl_b32 s20, s20, 6
	v_add_u32_e32 v9, s20, v5
	ds_read_b128 v[24:27], v9
	ds_read_b128 v[28:31], v9 offset:32
.Lgp_rn0:
	s_add_i32 s34, s34, 7
	s_cmp_gt_u32 s34, 31
	s_cbranch_scc1 .Lgp_rd_done
	s_cmp_gt_u32 s34, 15
	s_cbranch_scc1 .Lgp_rk1
	s_lshr_b32 s20, s34, 3
	s_mul_i32 s21, s20, 0x2200
	s_lshl_b32 s22, s34, 5
	s_and_b32 s22, s22, 0xe0
	s_add_i32 s21, s21, s22
	v_add_u32_e32 v8, s21, v2
	ds_read2_b64 v[36:39], v8 offset1:2
	s_lshl_b32 s20, s20, 7
	v_add_u32_e32 v9, s20, v3
	ds_read_b32 v40, v9
	s_branch .Lgp_rn1
.Lgp_rk1:
	s_and_b32 s20, s34, 3
	s_mul_i32 s21, s20, 0x1100
	s_bfe_u32 s22, s34, 0x20002
	s_lshl_b32 s23, s22, 6
	s_add_i32 s21, s21, s23
	v_add_u32_e32 v8, s21, v4
	ds_read_u16 v36, v8
	ds_read_u16 v37, v8 offset:272
	ds_read_u16 v38, v8 offset:544
	ds_read_u16 v39, v8 offset:816
	ds_read_u16 v40, v8 offset:2176
	ds_read_u16 v41, v8 offset:2448
	ds_read_u16 v42, v8 offset:2720
	ds_read_u16 v43, v8 offset:2992
	s_lshl_b32 s20, s20, 6
	v_add_u32_e32 v9, s20, v5
	ds_read_b128 v[44:47], v9
	ds_read_b128 v[48:51], v9 offset:32
.Lgp_rn1:
	s_add_i32 s34, s34, 7
	s_cmp_gt_u32 s34, 31
	s_cbranch_scc1 .Lgp_rd_done
	s_cmp_gt_u32 s34, 15
	s_cbranch_scc1 .Lgp_rk2
	s_lshr_b32 s20, s34, 3
	s_mul_i32 s21, s20, 0x2200
	s_lshl_b32 s22, s34, 5
	s_and_b32 s22, s22, 0xe0
	s_add_i32 s21, s21, s22
	v_add_u32_e32 v8, s21, v2
	ds_read2_b64 v[56:59], v8 offset1:2
	s_lshl_b32 s20, s20, 7
	v_add_u32_e32 v9, s20, v3
	ds_read_b32 v60, v9
	s_branch .Lgp_rn2
.Lgp_rk2:
	s_and_b32 s20, s34, 3
	s_mul_i32 s21, s20, 0x1100
	s_bfe_u32 s22, s34, 0x20002
	s_lshl_b32 s23, s22, 6
	s_add_i32 s21, s21, s23
	v_add_u32_e32 v8, s21, v4
	ds_read_u16 v56, v8
	ds_read_u16 v57, v8 offset:272
	ds_read_u16 v58, v8 offset:544
	ds_read_u16 v59, v8 offset:816
	ds_read_u16 v60, v8 offset:2176
	ds_read_u16 v61, v8 offset:2448
	ds_read_u16 v62, v8 offset:2720
	ds_read_u16 v63, v8 offset:2992
	s_lshl_b32 s20, s20, 6
	v_add_u32_e32 v9, s20, v5
	ds_read_b128 v[64:67], v9
	ds_read_b128 v[68:71], v9 offset:32
.Lgp_rn2:
	s_add_i32 s34, s34, 7
	s_cmp_gt_u32 s34, 31
	s_cbranch_scc1 .Lgp_rd_done
	s_cmp_gt_u32 s34, 15
	s_cbranch_scc1 .Lgp_rk3
	s_lshr_b32 s20, s34, 3
	s_mul_i32 s21, s20, 0x2200
	s_lshl_b32 s22, s34, 5
	s_and_b32 s22, s22, 0xe0
	s_add_i32 s21, s21, s22
	v_add_u32_e32 v8, s21, v2
	ds_read2_b64 v[76:79], v8 offset1:2
	s_lshl_b32 s20, s20, 7
	v_add_u32_e32 v9, s20, v3
	ds_read_b32 v80, v9
	s_branch .Lgp_rn3
.Lgp_rk3:
	s_and_b32 s20, s34, 3
	s_mul_i32 s21, s20, 0x1100
	s_bfe_u32 s22, s34, 0x20002
	s_lshl_b32 s23, s22, 6
	s_add_i32 s21, s21, s23
	v_add_u32_e32 v8, s21, v4
	ds_read_u16 v76, v8
	ds_read_u16 v77, v8 offset:272
	ds_read_u16 v78, v8 offset:544
	ds_read_u16 v79, v8 offset:816
	ds_read_u16 v80, v8 offset:2176
	ds_read_u16 v81, v8 offset:2448
	ds_read_u16 v82, v8 offset:2720
	ds_read_u16 v83, v8 offset:2992
	s_lshl_b32 s20, s20, 6
	v_add_u32_e32 v9, s20, v5
	ds_read_b128 v[84:87], v9
	ds_read_b128 v[88:91], v9 offset:32
.Lgp_rn3:
	s_add_i32 s34, s34, 7
	s_cmp_gt_u32 s34, 31
	s_cbranch_scc1 .Lgp_rd_done
	s_cmp_gt_u32 s34, 15
	s_cbranch_scc1 .Lgp_rk4
	s_lshr_b32 s20, s34, 3
	s_mul_i32 s21, s20, 0x2200
	s_lshl_b32 s22, s34, 5
	s_and_b32 s22, s22, 0xe0
	s_add_i32 s21, s21, s22
	v_add_u32_e32 v8, s21, v2
	ds_read2_b64 v[96:99], v8 offset1:2
	s_lshl_b32 s20, s20, 7
	v_add_u32_e32 v9, s20, v3
	ds_read_b32 v100, v9
	s_branch .Lgp_rn4
.Lgp_rk4:
	s_and_b32 s20, s34, 3
	s_mul_i32 s21, s20, 0x1100
	s_bfe_u32 s22, s34, 0x20002
	s_lshl_b32 s23, s22, 6
	s_add_i32 s21, s21, s23
	v_add_u32_e32 v8, s21, v4
	ds_read_u16 v96, v8
	ds_read_u16 v97, v8 offset:272
	ds_read_u16 v98, v8 offset:544
	ds_read_u16 v99, v8 offset:816
	ds_read_u16 v100, v8 offset:2176
	ds_read_u16 v101, v8 offset:2448
	ds_read_u16 v102, v8 offset:2720
	ds_read_u16 v103, v8 offset:2992
	s_lshl_b32 s20, s20, 6
	v_add_u32_e32 v9, s20, v5
	ds_read_b128 v[104:107], v9
	ds_read_b128 v[108:111], v9 offset:32
.Lgp_rn4:
.Lgp_rd_done:
	s_waitcnt lgkmcnt(0)
	s_add_i32 s34, s82, -1
	s_cmp_gt_u32 s34, 31
	s_cbranch_scc1 .LBB0_337
	s_lshl_b32 s20, s34, 10
	s_add_i32 s20, s20, 0x4000
	v_add_u32_e32 v8, s20, v6
	s_cmp_gt_u32 s34, 15
	s_cbranch_scc1 .Lgp_ck0
	v_lshlrev_b32_e32 v24, 16, v16
	v_and_b32_e32 v25, 0xffff0000, v16
	v_lshlrev_b32_e32 v26, 16, v17
	v_and_b32_e32 v27, 0xffff0000, v17
	v_lshlrev_b32_e32 v28, 16, v18
	v_and_b32_e32 v29, 0xffff0000, v18
	v_lshlrev_b32_e32 v30, 16, v19
	v_and_b32_e32 v31, 0xffff0000, v19
	v_mul_f32_e32 v24, v20, v24
	v_mul_f32_e32 v25, v20, v25
	v_mul_f32_e32 v26, v20, v26
	v_mul_f32_e32 v27, v20, v27
	v_mul_f32_e32 v28, v20, v28
	v_mul_f32_e32 v29, v20, v29
	v_mul_f32_e32 v30, v20, v30
	v_mul_f32_e32 v31, v20, v31
	v_cvt_pk_bf16_f32 v16, v24, v25
	v_cvt_pk_bf16_f32 v17, v26, v27
	v_cvt_pk_bf16_f32 v18, v28, v29
	v_cvt_pk_bf16_f32 v19, v30, v31
	global_store_dwordx4 v8, v[16:19], s[78:79]
	s_branch .Lgp_cn0
.Lgp_ck0:
	v_lshlrev_b32_e32 v16, 16, v16
	v_lshlrev_b32_e32 v17, 16, v17
	v_lshlrev_b32_e32 v18, 16, v18
	v_lshlrev_b32_e32 v19, 16, v19
	v_lshlrev_b32_e32 v20, 16, v20
	v_lshlrev_b32_e32 v21, 16, v21
	v_lshlrev_b32_e32 v22, 16, v22
	v_lshlrev_b32_e32 v23, 16, v23
	v_mul_f32_e32 v16, v24, v16
	v_mul_f32_e32 v17, v25, v17
	v_mul_f32_e32 v18, v26, v18
	v_mul_f32_e32 v19, v27, v19
	v_mul_f32_e32 v20, v28, v20
	v_mul_f32_e32 v21, v29, v21
	v_mul_f32_e32 v22, v30, v22
	v_mul_f32_e32 v23, v31, v23
	v_cvt_pk_bf16_f32 v32, v16, v17
	v_cvt_pk_bf16_f32 v33, v18, v19
	v_cvt_pk_bf16_f32 v34, v20, v21
	v_cvt_pk_bf16_f32 v35, v22, v23
	global_store_dwordx4 v8, v[32:35], s[78:79]
.Lgp_cn0:
	s_add_i32 s34, s34, 7
	s_cmp_gt_u32 s34, 31
	s_cbranch_scc1 .LBB0_337
	s_lshl_b32 s20, s34, 10
	s_add_i32 s20, s20, 0x4000
	v_add_u32_e32 v8, s20, v6
	s_cmp_gt_u32 s34, 15
	s_cbranch_scc1 .Lgp_ck1
	v_lshlrev_b32_e32 v44, 16, v36
	v_and_b32_e32 v45, 0xffff0000, v36
	v_lshlrev_b32_e32 v46, 16, v37
	v_and_b32_e32 v47, 0xffff0000, v37
	v_lshlrev_b32_e32 v48, 16, v38
	v_and_b32_e32 v49, 0xffff0000, v38
	v_lshlrev_b32_e32 v50, 16, v39
	v_and_b32_e32 v51, 0xffff0000, v39
	v_mul_f32_e32 v44, v40, v44
	v_mul_f32_e32 v45, v40, v45
	v_mul_f32_e32 v46, v40, v46
	v_mul_f32_e32 v47, v40, v47
	v_mul_f32_e32 v48, v40, v48
	v_mul_f32_e32 v49, v40, v49
	v_mul_f32_e32 v50, v40, v50
	v_mul_f32_e32 v51, v40, v51
	v_cvt_pk_bf16_f32 v36, v44, v45
	v_cvt_pk_bf16_f32 v37, v46, v47
	v_cvt_pk_bf16_f32 v38, v48, v49
	v_cvt_pk_bf16_f32 v39, v50, v51
	global_store_dwordx4 v8, v[36:39], s[78:79]
	s_branch .Lgp_cn1
.Lgp_ck1:
	v_lshlrev_b32_e32 v36, 16, v36
	v_lshlrev_b32_e32 v37, 16, v37
	v_lshlrev_b32_e32 v38, 16, v38
	v_lshlrev_b32_e32 v39, 16, v39
	v_lshlrev_b32_e32 v40, 16, v40
	v_lshlrev_b32_e32 v41, 16, v41
	v_lshlrev_b32_e32 v42, 16, v42
	v_lshlrev_b32_e32 v43, 16, v43
	v_mul_f32_e32 v36, v44, v36
	v_mul_f32_e32 v37, v45, v37
	v_mul_f32_e32 v38, v46, v38
	v_mul_f32_e32 v39, v47, v39
	v_mul_f32_e32 v40, v48, v40
	v_mul_f32_e32 v41, v49, v41
	v_mul_f32_e32 v42, v50, v42
	v_mul_f32_e32 v43, v51, v43
	v_cvt_pk_bf16_f32 v52, v36, v37
	v_cvt_pk_bf16_f32 v53, v38, v39
	v_cvt_pk_bf16_f32 v54, v40, v41
	v_cvt_pk_bf16_f32 v55, v42, v43
	global_store_dwordx4 v8, v[52:55], s[78:79]
.Lgp_cn1:
	s_add_i32 s34, s34, 7
	s_cmp_gt_u32 s34, 31
	s_cbranch_scc1 .LBB0_337
	s_lshl_b32 s20, s34, 10
	s_add_i32 s20, s20, 0x4000
	v_add_u32_e32 v8, s20, v6
	s_cmp_gt_u32 s34, 15
	s_cbranch_scc1 .Lgp_ck2
	v_lshlrev_b32_e32 v64, 16, v56
	v_and_b32_e32 v65, 0xffff0000, v56
	v_lshlrev_b32_e32 v66, 16, v57
	v_and_b32_e32 v67, 0xffff0000, v57
	v_lshlrev_b32_e32 v68, 16, v58
	v_and_b32_e32 v69, 0xffff0000, v58
	v_lshlrev_b32_e32 v70, 16, v59
	v_and_b32_e32 v71, 0xffff0000, v59
	v_mul_f32_e32 v64, v60, v64
	v_mul_f32_e32 v65, v60, v65
	v_mul_f32_e32 v66, v60, v66
	v_mul_f32_e32 v67, v60, v67
	v_mul_f32_e32 v68, v60, v68
	v_mul_f32_e32 v69, v60, v69
	v_mul_f32_e32 v70, v60, v70
	v_mul_f32_e32 v71, v60, v71
	v_cvt_pk_bf16_f32 v56, v64, v65
	v_cvt_pk_bf16_f32 v57, v66, v67
	v_cvt_pk_bf16_f32 v58, v68, v69
	v_cvt_pk_bf16_f32 v59, v70, v71
	global_store_dwordx4 v8, v[56:59], s[78:79]
	s_branch .Lgp_cn2
.Lgp_ck2:
	v_lshlrev_b32_e32 v56, 16, v56
	v_lshlrev_b32_e32 v57, 16, v57
	v_lshlrev_b32_e32 v58, 16, v58
	v_lshlrev_b32_e32 v59, 16, v59
	v_lshlrev_b32_e32 v60, 16, v60
	v_lshlrev_b32_e32 v61, 16, v61
	v_lshlrev_b32_e32 v62, 16, v62
	v_lshlrev_b32_e32 v63, 16, v63
	v_mul_f32_e32 v56, v64, v56
	v_mul_f32_e32 v57, v65, v57
	v_mul_f32_e32 v58, v66, v58
	v_mul_f32_e32 v59, v67, v59
	v_mul_f32_e32 v60, v68, v60
	v_mul_f32_e32 v61, v69, v61
	v_mul_f32_e32 v62, v70, v62
	v_mul_f32_e32 v63, v71, v63
	v_cvt_pk_bf16_f32 v72, v56, v57
	v_cvt_pk_bf16_f32 v73, v58, v59
	v_cvt_pk_bf16_f32 v74, v60, v61
	v_cvt_pk_bf16_f32 v75, v62, v63
	global_store_dwordx4 v8, v[72:75], s[78:79]
.Lgp_cn2:
	s_add_i32 s34, s34, 7
	s_cmp_gt_u32 s34, 31
	s_cbranch_scc1 .LBB0_337
	s_lshl_b32 s20, s34, 10
	s_add_i32 s20, s20, 0x4000
	v_add_u32_e32 v8, s20, v6
	s_cmp_gt_u32 s34, 15
	s_cbranch_scc1 .Lgp_ck3
	v_lshlrev_b32_e32 v84, 16, v76
	v_and_b32_e32 v85, 0xffff0000, v76
	v_lshlrev_b32_e32 v86, 16, v77
	v_and_b32_e32 v87, 0xffff0000, v77
	v_lshlrev_b32_e32 v88, 16, v78
	v_and_b32_e32 v89, 0xffff0000, v78
	v_lshlrev_b32_e32 v90, 16, v79
	v_and_b32_e32 v91, 0xffff0000, v79
	v_mul_f32_e32 v84, v80, v84
	v_mul_f32_e32 v85, v80, v85
	v_mul_f32_e32 v86, v80, v86
	v_mul_f32_e32 v87, v80, v87
	v_mul_f32_e32 v88, v80, v88
	v_mul_f32_e32 v89, v80, v89
	v_mul_f32_e32 v90, v80, v90
	v_mul_f32_e32 v91, v80, v91
	v_cvt_pk_bf16_f32 v76, v84, v85
	v_cvt_pk_bf16_f32 v77, v86, v87
	v_cvt_pk_bf16_f32 v78, v88, v89
	v_cvt_pk_bf16_f32 v79, v90, v91
	global_store_dwordx4 v8, v[76:79], s[78:79]
	s_branch .Lgp_cn3
.Lgp_ck3:
	v_lshlrev_b32_e32 v76, 16, v76
	v_lshlrev_b32_e32 v77, 16, v77
	v_lshlrev_b32_e32 v78, 16, v78
	v_lshlrev_b32_e32 v79, 16, v79
	v_lshlrev_b32_e32 v80, 16, v80
	v_lshlrev_b32_e32 v81, 16, v81
	v_lshlrev_b32_e32 v82, 16, v82
	v_lshlrev_b32_e32 v83, 16, v83
	v_mul_f32_e32 v76, v84, v76
	v_mul_f32_e32 v77, v85, v77
	v_mul_f32_e32 v78, v86, v78
	v_mul_f32_e32 v79, v87, v79
	v_mul_f32_e32 v80, v88, v80
	v_mul_f32_e32 v81, v89, v81
	v_mul_f32_e32 v82, v90, v82
	v_mul_f32_e32 v83, v91, v83
	v_cvt_pk_bf16_f32 v92, v76, v77
	v_cvt_pk_bf16_f32 v93, v78, v79
	v_cvt_pk_bf16_f32 v94, v80, v81
	v_cvt_pk_bf16_f32 v95, v82, v83
	global_store_dwordx4 v8, v[92:95], s[78:79]
.Lgp_cn3:
	s_add_i32 s34, s34, 7
	s_cmp_gt_u32 s34, 31
	s_cbranch_scc1 .LBB0_337
	s_lshl_b32 s20, s34, 10
	s_add_i32 s20, s20, 0x4000
	v_add_u32_e32 v8, s20, v6
	s_cmp_gt_u32 s34, 15
	s_cbranch_scc1 .Lgp_ck4
	v_lshlrev_b32_e32 v104, 16, v96
	v_and_b32_e32 v105, 0xffff0000, v96
	v_lshlrev_b32_e32 v106, 16, v97
	v_and_b32_e32 v107, 0xffff0000, v97
	v_lshlrev_b32_e32 v108, 16, v98
	v_and_b32_e32 v109, 0xffff0000, v98
	v_lshlrev_b32_e32 v110, 16, v99
	v_and_b32_e32 v111, 0xffff0000, v99
	v_mul_f32_e32 v104, v100, v104
	v_mul_f32_e32 v105, v100, v105
	v_mul_f32_e32 v106, v100, v106
	v_mul_f32_e32 v107, v100, v107
	v_mul_f32_e32 v108, v100, v108
	v_mul_f32_e32 v109, v100, v109
	v_mul_f32_e32 v110, v100, v110
	v_mul_f32_e32 v111, v100, v111
	v_cvt_pk_bf16_f32 v96, v104, v105
	v_cvt_pk_bf16_f32 v97, v106, v107
	v_cvt_pk_bf16_f32 v98, v108, v109
	v_cvt_pk_bf16_f32 v99, v110, v111
	global_store_dwordx4 v8, v[96:99], s[78:79]
	s_branch .Lgp_cn4
.Lgp_ck4:
	v_lshlrev_b32_e32 v96, 16, v96
	v_lshlrev_b32_e32 v97, 16, v97
	v_lshlrev_b32_e32 v98, 16, v98
	v_lshlrev_b32_e32 v99, 16, v99
	v_lshlrev_b32_e32 v100, 16, v100
	v_lshlrev_b32_e32 v101, 16, v101
	v_lshlrev_b32_e32 v102, 16, v102
	v_lshlrev_b32_e32 v103, 16, v103
	v_mul_f32_e32 v96, v104, v96
	v_mul_f32_e32 v97, v105, v97
	v_mul_f32_e32 v98, v106, v98
	v_mul_f32_e32 v99, v107, v99
	v_mul_f32_e32 v100, v108, v100
	v_mul_f32_e32 v101, v109, v101
	v_mul_f32_e32 v102, v110, v102
	v_mul_f32_e32 v103, v111, v103
	v_cvt_pk_bf16_f32 v112, v96, v97
	v_cvt_pk_bf16_f32 v113, v98, v99
	v_cvt_pk_bf16_f32 v114, v100, v101
	v_cvt_pk_bf16_f32 v115, v102, v103
	global_store_dwordx4 v8, v[112:115], s[78:79]
.Lgp_cn4:
.LBB0_337:
	s_or_b64 exec, exec, s[0:1]
	s_mov_b64 s[0:1], 0
